# MoeOrder::next (M1/M2 unit loop top): expert index from one per-lane LDS read + v_cmp + s_bcnt1 instead of 15 serial LDS round trips; on top of m10
# speedup vs baseline: 1.0190x; 1.0020x over previous
; DI int rfl(int v) { return __builtin_amdgcn_readfirstlane(v); }
;     DI bool next(int i, Unit& u) const {
;         const int L = i * G + c; if (L >= ntot) return false;
;         const int rt = L / NC; u.pn = L - rt * NC; u.pm = rt;
;         int e = 0;
; #pragma unroll
;         for (int j = 1; j < 16; ++j) e += (rt >= rfl(pre[j])) ? 1 : 0;
;         e = rfl(e); u.e = e; const int rem = rfl(cnt[e]) - 256 * (rt - rfl(pre[e])); u.nv = rem < 256 ? rem : 256; u.ui = i; return true;
.LBB0_1357:
	s_add_i32 s89, s89, 1
	s_mul_i32 s6, s89, s39
	s_add_i32 s6, s6, s78
	s_cmp_lt_i32 s6, s79
	s_cselect_b64 s[74:75], -1, 0
	s_cmp_ge_i32 s6, s79
	s_cbranch_scc1 .LBB0_1359
	s_ashr_i32 s7, s6, 31
	s_lshr_b32 s7, s7, 29
	v_lshl_add_u32 v6, v202, 2, s76
	ds_read_b32 v6, v6
	s_add_i32 s7, s6, s7
	s_ashr_i32 s92, s7, 3
	s_and_b32 s7, s7, -8
	s_sub_i32 s66, s6, s7
	s_mov_b32 s91, s89
	s_waitcnt lgkmcnt(0)
	v_cmp_le_i32_e64 s[6:7], v6, s92
	s_and_b32 s6, s6, 0xfffe
	s_bcnt1_i32_b32 s56, s6
	s_lshl_b32 s6, s56, 2
	s_add_i32 s7, s13, s6
	v_mov_b32_e32 v6, s7
	ds_read_b32 v6, v6
	s_add_i32 s6, s76, s6
	s_waitcnt lgkmcnt(0)
	v_mov_b32_e32 v6, s6
	ds_read_b32 v6, v6

; DI int rfl(int v) { return __builtin_amdgcn_readfirstlane(v); }
;     DI bool next(int i, Unit& u) const {
;         const int L = i * G + c; if (L >= ntot) return false;
;         const int rt = L / NC; u.pn = L - rt * NC; u.pm = rt;
;         int e = 0;
; #pragma unroll
;         for (int j = 1; j < 16; ++j) e += (rt >= rfl(pre[j])) ? 1 : 0;
;         e = rfl(e); u.e = e; const int rem = rfl(cnt[e]) - 256 * (rt - rfl(pre[e])); u.nv = rem < 256 ? rem : 256; u.ui = i; return true;
.LBB0_1636:
	s_add_i32 s92, s92, 1
	s_mul_i32 s0, s92, s13
	s_add_i32 s0, s0, s68
	s_cmp_lt_i32 s0, s76
	s_cselect_b64 s[46:47], -1, 0
	s_cmp_ge_i32 s0, s76
	s_cbranch_scc1 .LBB0_1638
	s_ashr_i32 s1, s0, 31
	s_lshr_b32 s1, s1, 30
	v_lshl_add_u32 v6, v202, 2, s39
	ds_read_b32 v6, v6
	s_add_i32 s1, s0, s1
	s_ashr_i32 s16, s1, 2
	s_and_b32 s1, s1, -4
	s_sub_i32 s74, s0, s1
	s_waitcnt lgkmcnt(0)
	v_cmp_le_i32_e64 s[0:1], v6, s16
	s_and_b32 s0, s0, 0xfffe
	s_bcnt1_i32_b32 s60, s0
	s_lshl_b32 s0, s60, 2
	s_add_i32 s1, s2, s0
	s_add_i32 s0, s39, s0
	v_mov_b32_e32 v6, s1
	v_mov_b32_e32 v7, s0
	ds_read_b32 v6, v6
	ds_read_b32 v7, v7
	s_waitcnt lgkmcnt(0)
	v_readfirstlane_b32 s0, v6
	v_readfirstlane_b32 s1, v7
	s_sub_i32 s1, s1, s16
	s_lshl_b32 s1, s1, 8
	s_add_i32 s1, s1, s0
	s_min_i32 s94, s1, 0x100
